# merge hook stores widened: the two 16-column halves exchanged with v_permlane16_swap so each lane stores 16 bytes (64 contiguous bytes per row) instead of two 8-byte stores
# speedup vs baseline: 1.0095x; 1.0095x over previous
; __device__ __forceinline__ unsigned cvtpk(float lo, float hi) { f32x2_t v = {lo, hi}; bf16x2_t b = __builtin_convertvector(v, bf16x2_t); return __builtin_bit_cast(unsigned, b); }
; __device__ __forceinline__ float bflo(unsigned w) { return __uint_as_float(w << 16); }
; __device__ __forceinline__ float bfhi(unsigned w) { return __uint_as_float(w & 0xffff0000u); }
; __device__ __forceinline__ int tid_opaque() { int t = threadIdx.x; asm volatile("" : "+v"(t)); return t; }
; __device__ __forceinline__ void phase_merge(const Ptrs& p, LAS unsigned char* lds) {
;     ...
;             const int tid = tid_opaque(), wid = tid >> 6, lane = tid & 63, wr = wid >> 2, wc = wid & 3, fr = lane & 15, fq = lane >> 4;
; #pragma unroll
;             for (int ai = 0; ai < 2; ++ai)
; #pragma unroll
;                 for (int m = 0; m < 4; ++m) { const int row = row0 + ai * 128 + wr * 64 + m * 16 + fr;
; #pragma unroll
;                     for (int bj = 0; bj < 2; ++bj)
; #pragma unroll
;                         for (int n = 0; n < 2; ++n) { const int c = col0 + bj * 128 + wc * 32 + n * 16 + fq * 4; const size_t o = (size_t)row * PLD + c;
;                             const u32x2 sa = *(const u32x2*)(pr + o + C_GA); u32x2 sc = sa; if (seg == 0) sc = *(const u32x2*)(pr + o + C_GC);
;                             f32x4 v = acc[ai][bj][m][n];
;                             const float a0 = bflo(sa.x), a1 = bfhi(sa.x), a2 = bflo(sa.y), a3 = bfhi(sa.y);
;                             if (seg == 0) { v[0] *= bflo(sc.x) * __builtin_amdgcn_rcpf(a0); v[1] *= bfhi(sc.x) * __builtin_amdgcn_rcpf(a1); v[2] *= bflo(sc.y) * __builtin_amdgcn_rcpf(a2); v[3] *= bfhi(sc.y) * __builtin_amdgcn_rcpf(a3); }
;                             else { v[0] *= a0; v[1] *= a1; v[2] *= a2; v[3] *= a3; }
;                             acc[ai][bj][m][n] = v;
;                             if (seg == 1) { u32x2 w; w.x = cvtpk(v[0], v[1]); w.y = cvtpk(v[2], v[3]); *(u32x2*)(mg + (size_t)row * D + c) = w; } }
;                     asm volatile("" ::: "memory"); }
.Lmy_mg_seg1:
	global_load_dwordx2 v[148:149], v[212:213], off offset:2048
	global_load_dwordx2 v[150:151], v[212:213], off offset:2080
	global_load_dwordx2 v[152:153], v[212:213], off offset:2304
	global_load_dwordx2 v[154:155], v[212:213], off offset:2336
	global_load_dwordx2 v[156:157], v[214:215], off offset:2048
	global_load_dwordx2 v[158:159], v[214:215], off offset:2080
	global_load_dwordx2 v[160:161], v[214:215], off offset:2304
	global_load_dwordx2 v[162:163], v[214:215], off offset:2336
	global_load_dwordx2 v[164:165], v[216:217], off offset:2048
	global_load_dwordx2 v[166:167], v[216:217], off offset:2080
	global_load_dwordx2 v[168:169], v[216:217], off offset:2304
	global_load_dwordx2 v[170:171], v[216:217], off offset:2336
	global_load_dwordx2 v[172:173], v[218:219], off offset:2048
	global_load_dwordx2 v[174:175], v[218:219], off offset:2080
	global_load_dwordx2 v[176:177], v[218:219], off offset:2304
	global_load_dwordx2 v[178:179], v[218:219], off offset:2336
	global_load_dwordx2 v[180:181], v[220:221], off offset:2048
	global_load_dwordx2 v[182:183], v[220:221], off offset:2080
	global_load_dwordx2 v[184:185], v[220:221], off offset:2304
	global_load_dwordx2 v[186:187], v[220:221], off offset:2336
	global_load_dwordx2 v[188:189], v[222:223], off offset:2048
	global_load_dwordx2 v[190:191], v[222:223], off offset:2080
	global_load_dwordx2 v[192:193], v[222:223], off offset:2304
	global_load_dwordx2 v[194:195], v[222:223], off offset:2336
	global_load_dwordx2 v[196:197], v[224:225], off offset:2048
	global_load_dwordx2 v[198:199], v[224:225], off offset:2080
	global_load_dwordx2 v[200:201], v[224:225], off offset:2304
	global_load_dwordx2 v[202:203], v[224:225], off offset:2336
	global_load_dwordx2 v[204:205], v[226:227], off offset:2048
	global_load_dwordx2 v[206:207], v[226:227], off offset:2080
	global_load_dwordx2 v[208:209], v[226:227], off offset:2304
	global_load_dwordx2 v[210:211], v[226:227], off offset:2336
	v_bfe_u32 v252, v0, 4, 1
	v_mul_u32_u24_e32 v252, 24, v252
	v_add_u32_e32 v252, v252, v2
	v_mov_b32_e32 v253, 0
	v_mov_b32_e32 v139, 0
	v_mov_b32_e32 v138, v136
	v_lshlrev_b64 v[228:229], 12, v[138:139]
	v_lshl_add_u64 v[228:229], s[12:13], 0, v[228:229]
	v_lshl_add_u64 v[228:229], v[228:229], 0, v[252:253]
	v_add_u32_e32 v138, 0x10, v136
	v_lshlrev_b64 v[230:231], 12, v[138:139]
	v_lshl_add_u64 v[230:231], s[12:13], 0, v[230:231]
	v_lshl_add_u64 v[230:231], v[230:231], 0, v[252:253]
	v_add_u32_e32 v138, 0x20, v136
	v_lshlrev_b64 v[232:233], 12, v[138:139]
	v_lshl_add_u64 v[232:233], s[12:13], 0, v[232:233]
	v_lshl_add_u64 v[232:233], v[232:233], 0, v[252:253]
	v_add_u32_e32 v138, 0x30, v136
	v_lshlrev_b64 v[234:235], 12, v[138:139]
	v_lshl_add_u64 v[234:235], s[12:13], 0, v[234:235]
	v_lshl_add_u64 v[234:235], v[234:235], 0, v[252:253]
	v_add_u32_e32 v138, 0x80, v136
	v_lshlrev_b64 v[236:237], 12, v[138:139]
	v_lshl_add_u64 v[236:237], s[12:13], 0, v[236:237]
	v_lshl_add_u64 v[236:237], v[236:237], 0, v[252:253]
	v_add_u32_e32 v138, 0x90, v136
	v_lshlrev_b64 v[238:239], 12, v[138:139]
	v_lshl_add_u64 v[238:239], s[12:13], 0, v[238:239]
	v_lshl_add_u64 v[238:239], v[238:239], 0, v[252:253]
	v_add_u32_e32 v138, 0xa0, v136
	v_lshlrev_b64 v[240:241], 12, v[138:139]
	v_lshl_add_u64 v[240:241], s[12:13], 0, v[240:241]
	v_lshl_add_u64 v[240:241], v[240:241], 0, v[252:253]
	v_add_u32_e32 v138, 0xb0, v136
	v_lshlrev_b64 v[242:243], 12, v[138:139]
	v_lshl_add_u64 v[242:243], s[12:13], 0, v[242:243]
	v_lshl_add_u64 v[242:243], v[242:243], 0, v[252:253]
	s_waitcnt vmcnt(0)
	v_lshlrev_b32_e32 v140, 16, v148
	v_and_b32_e32 v141, 0xffff0000, v148
	v_lshlrev_b32_e32 v142, 16, v149
	v_and_b32_e32 v143, 0xffff0000, v149
	v_mul_f32_e32 v4, v8, v140
	v_mul_f32_e32 v5, v9, v141
	v_mul_f32_e32 v6, v10, v142
	v_mul_f32_e32 v7, v11, v143
	v_lshlrev_b32_e32 v140, 16, v150
	v_and_b32_e32 v141, 0xffff0000, v150
	v_lshlrev_b32_e32 v142, 16, v151
	v_and_b32_e32 v143, 0xffff0000, v151
	v_mul_f32_e32 v8, v12, v140
	v_mul_f32_e32 v9, v13, v141
	v_mul_f32_e32 v10, v14, v142
	v_mul_f32_e32 v11, v15, v143
	s_nop 1
	v_permlane16_swap_b32_e32 v4, v8
	v_permlane16_swap_b32_e32 v5, v9
	v_permlane16_swap_b32_e32 v6, v10
	v_permlane16_swap_b32_e32 v7, v11
	v_cvt_pk_bf16_f32 v136, v4, v5
	v_cvt_pk_bf16_f32 v137, v6, v7
	v_cvt_pk_bf16_f32 v138, v8, v9
	v_cvt_pk_bf16_f32 v139, v10, v11
	global_store_dwordx4 v[228:229], v[136:139], off
	v_lshlrev_b32_e32 v140, 16, v152
	v_and_b32_e32 v141, 0xffff0000, v152
	v_lshlrev_b32_e32 v142, 16, v153
	v_and_b32_e32 v143, 0xffff0000, v153
	v_mul_f32_e32 v12, v16, v140
	v_mul_f32_e32 v13, v17, v141
	v_mul_f32_e32 v14, v18, v142
	v_mul_f32_e32 v15, v19, v143
	v_lshlrev_b32_e32 v140, 16, v154
	v_and_b32_e32 v141, 0xffff0000, v154
	v_lshlrev_b32_e32 v142, 16, v155
	v_and_b32_e32 v143, 0xffff0000, v155
	v_mul_f32_e32 v16, v24, v140
	v_mul_f32_e32 v17, v25, v141
	v_mul_f32_e32 v18, v26, v142
	v_mul_f32_e32 v19, v27, v143
	s_nop 1
	v_permlane16_swap_b32_e32 v12, v16
	v_permlane16_swap_b32_e32 v13, v17
	v_permlane16_swap_b32_e32 v14, v18
	v_permlane16_swap_b32_e32 v15, v19
	v_cvt_pk_bf16_f32 v144, v12, v13
	v_cvt_pk_bf16_f32 v145, v14, v15
	v_cvt_pk_bf16_f32 v146, v16, v17
	v_cvt_pk_bf16_f32 v147, v18, v19
	global_store_dwordx4 v[228:229], v[144:147], off offset:256
	v_lshlrev_b32_e32 v140, 16, v156
	v_and_b32_e32 v141, 0xffff0000, v156
	v_lshlrev_b32_e32 v142, 16, v157
	v_and_b32_e32 v143, 0xffff0000, v157
	v_mul_f32_e32 v24, v36, v140
	v_mul_f32_e32 v25, v37, v141
	v_mul_f32_e32 v26, v38, v142
	v_mul_f32_e32 v27, v39, v143
	v_lshlrev_b32_e32 v140, 16, v158
	v_and_b32_e32 v141, 0xffff0000, v158
	v_lshlrev_b32_e32 v142, 16, v159
; __device__ __forceinline__ unsigned cvtpk(float lo, float hi) { f32x2_t v = {lo, hi}; bf16x2_t b = __builtin_convertvector(v, bf16x2_t); return __builtin_bit_cast(unsigned, b); }
; __device__ __forceinline__ float bflo(unsigned w) { return __uint_as_float(w << 16); }
; __device__ __forceinline__ float bfhi(unsigned w) { return __uint_as_float(w & 0xffff0000u); }
; __device__ __forceinline__ void phase_merge(const Ptrs& p, LAS unsigned char* lds) {
;     ...
;                 for (int m = 0; m < 4; ++m) { const int row = row0 + ai * 128 + wr * 64 + m * 16 + fr;
; #pragma unroll
;                     for (int bj = 0; bj < 2; ++bj)
; #pragma unroll
;                         for (int n = 0; n < 2; ++n) { const int c = col0 + bj * 128 + wc * 32 + n * 16 + fq * 4; const size_t o = (size_t)row * PLD + c;
;                             const u32x2 sa = *(const u32x2*)(pr + o + C_GA); u32x2 sc = sa; if (seg == 0) sc = *(const u32x2*)(pr + o + C_GC);
;                             f32x4 v = acc[ai][bj][m][n];
;                             const float a0 = bflo(sa.x), a1 = bfhi(sa.x), a2 = bflo(sa.y), a3 = bfhi(sa.y);
;                             if (seg == 0) { v[0] *= bflo(sc.x) * __builtin_amdgcn_rcpf(a0); v[1] *= bfhi(sc.x) * __builtin_amdgcn_rcpf(a1); v[2] *= bflo(sc.y) * __builtin_amdgcn_rcpf(a2); v[3] *= bfhi(sc.y) * __builtin_amdgcn_rcpf(a3); }
;                             else { v[0] *= a0; v[1] *= a1; v[2] *= a2; v[3] *= a3; }
;                             acc[ai][bj][m][n] = v;
;                             if (seg == 1) { u32x2 w; w.x = cvtpk(v[0], v[1]); w.y = cvtpk(v[2], v[3]); *(u32x2*)(mg + (size_t)row * D + c) = w; } }
;                     asm volatile("" ::: "memory"); }
	v_and_b32_e32 v143, 0xffff0000, v159
	v_mul_f32_e32 v36, v40, v140
	v_mul_f32_e32 v37, v41, v141
	v_mul_f32_e32 v38, v42, v142
	v_mul_f32_e32 v39, v43, v143
	s_nop 1
	v_permlane16_swap_b32_e32 v24, v36
	v_permlane16_swap_b32_e32 v25, v37
	v_permlane16_swap_b32_e32 v26, v38
	v_permlane16_swap_b32_e32 v27, v39
	v_cvt_pk_bf16_f32 v136, v24, v25
	v_cvt_pk_bf16_f32 v137, v26, v27
	v_cvt_pk_bf16_f32 v138, v36, v37
	v_cvt_pk_bf16_f32 v139, v38, v39
	global_store_dwordx4 v[230:231], v[136:139], off
	v_lshlrev_b32_e32 v140, 16, v160
	v_and_b32_e32 v141, 0xffff0000, v160
	v_lshlrev_b32_e32 v142, 16, v161
	v_and_b32_e32 v143, 0xffff0000, v161
	v_mul_f32_e32 v40, v48, v140
	v_mul_f32_e32 v41, v49, v141
	v_mul_f32_e32 v42, v50, v142
	v_mul_f32_e32 v43, v51, v143
	v_lshlrev_b32_e32 v140, 16, v162
	v_and_b32_e32 v141, 0xffff0000, v162
	v_lshlrev_b32_e32 v142, 16, v163
	v_and_b32_e32 v143, 0xffff0000, v163
	v_mul_f32_e32 v48, v56, v140
	v_mul_f32_e32 v49, v57, v141
	v_mul_f32_e32 v50, v58, v142
	v_mul_f32_e32 v51, v59, v143
	s_nop 1
	v_permlane16_swap_b32_e32 v40, v48
	v_permlane16_swap_b32_e32 v41, v49
	v_permlane16_swap_b32_e32 v42, v50
	v_permlane16_swap_b32_e32 v43, v51
	v_cvt_pk_bf16_f32 v144, v40, v41
	v_cvt_pk_bf16_f32 v145, v42, v43
	v_cvt_pk_bf16_f32 v146, v48, v49
	v_cvt_pk_bf16_f32 v147, v50, v51
	global_store_dwordx4 v[230:231], v[144:147], off offset:256
	v_lshlrev_b32_e32 v140, 16, v164
	v_and_b32_e32 v141, 0xffff0000, v164
	v_lshlrev_b32_e32 v142, 16, v165
	v_and_b32_e32 v143, 0xffff0000, v165
	v_mul_f32_e32 v56, v68, v140
	v_mul_f32_e32 v57, v69, v141
	v_mul_f32_e32 v58, v70, v142
	v_mul_f32_e32 v59, v71, v143
	v_lshlrev_b32_e32 v140, 16, v166
	v_and_b32_e32 v141, 0xffff0000, v166
	v_lshlrev_b32_e32 v142, 16, v167
	v_and_b32_e32 v143, 0xffff0000, v167
	v_mul_f32_e32 v68, v72, v140
	v_mul_f32_e32 v69, v73, v141
	v_mul_f32_e32 v70, v74, v142
	v_mul_f32_e32 v71, v75, v143
	s_nop 1
	v_permlane16_swap_b32_e32 v56, v68
	v_permlane16_swap_b32_e32 v57, v69
	v_permlane16_swap_b32_e32 v58, v70
	v_permlane16_swap_b32_e32 v59, v71
	v_cvt_pk_bf16_f32 v136, v56, v57
	v_cvt_pk_bf16_f32 v137, v58, v59
	v_cvt_pk_bf16_f32 v138, v68, v69
	v_cvt_pk_bf16_f32 v139, v70, v71
	global_store_dwordx4 v[232:233], v[136:139], off
	v_lshlrev_b32_e32 v140, 16, v168
	v_and_b32_e32 v141, 0xffff0000, v168
	v_lshlrev_b32_e32 v142, 16, v169
	v_and_b32_e32 v143, 0xffff0000, v169
	v_mul_f32_e32 v72, v80, v140
	v_mul_f32_e32 v73, v81, v141
	v_mul_f32_e32 v74, v82, v142
	v_mul_f32_e32 v75, v83, v143
	v_lshlrev_b32_e32 v140, 16, v170
	v_and_b32_e32 v141, 0xffff0000, v170
	v_lshlrev_b32_e32 v142, 16, v171
	v_and_b32_e32 v143, 0xffff0000, v171
	v_mul_f32_e32 v80, v88, v140
	v_mul_f32_e32 v81, v89, v141
	v_mul_f32_e32 v82, v90, v142
	v_mul_f32_e32 v83, v91, v143
	s_nop 1
	v_permlane16_swap_b32_e32 v72, v80
	v_permlane16_swap_b32_e32 v73, v81
	v_permlane16_swap_b32_e32 v74, v82
	v_permlane16_swap_b32_e32 v75, v83
	v_cvt_pk_bf16_f32 v144, v72, v73
	v_cvt_pk_bf16_f32 v145, v74, v75
	v_cvt_pk_bf16_f32 v146, v80, v81
	v_cvt_pk_bf16_f32 v147, v82, v83
	global_store_dwordx4 v[232:233], v[144:147], off offset:256
	v_lshlrev_b32_e32 v140, 16, v172
	v_and_b32_e32 v141, 0xffff0000, v172
	v_lshlrev_b32_e32 v142, 16, v173
	v_and_b32_e32 v143, 0xffff0000, v173
	v_mul_f32_e32 v88, v100, v140
	v_mul_f32_e32 v89, v101, v141
	v_mul_f32_e32 v90, v102, v142
	v_mul_f32_e32 v91, v103, v143
	v_lshlrev_b32_e32 v140, 16, v174
	v_and_b32_e32 v141, 0xffff0000, v174
	v_lshlrev_b32_e32 v142, 16, v175
	v_and_b32_e32 v143, 0xffff0000, v175
	v_mul_f32_e32 v100, v104, v140
	v_mul_f32_e32 v101, v105, v141
	v_mul_f32_e32 v102, v106, v142
	v_mul_f32_e32 v103, v107, v143
	s_nop 1
	v_permlane16_swap_b32_e32 v88, v100
	v_permlane16_swap_b32_e32 v89, v101
	v_permlane16_swap_b32_e32 v90, v102
	v_permlane16_swap_b32_e32 v91, v103
	v_cvt_pk_bf16_f32 v136, v88, v89
	v_cvt_pk_bf16_f32 v137, v90, v91
	v_cvt_pk_bf16_f32 v138, v100, v101
	v_cvt_pk_bf16_f32 v139, v102, v103
	global_store_dwordx4 v[234:235], v[136:139], off
	v_lshlrev_b32_e32 v140, 16, v176
	v_and_b32_e32 v141, 0xffff0000, v176
	v_lshlrev_b32_e32 v142, 16, v177
	v_and_b32_e32 v143, 0xffff0000, v177
	v_mul_f32_e32 v104, v112, v140
	v_mul_f32_e32 v105, v113, v141
	v_mul_f32_e32 v106, v114, v142
	v_mul_f32_e32 v107, v115, v143
	v_lshlrev_b32_e32 v140, 16, v178
	v_and_b32_e32 v141, 0xffff0000, v178
	v_lshlrev_b32_e32 v142, 16, v179
	v_and_b32_e32 v143, 0xffff0000, v179
	v_mul_f32_e32 v112, v120, v140
	v_mul_f32_e32 v113, v121, v141
	v_mul_f32_e32 v114, v122, v142
	v_mul_f32_e32 v115, v123, v143
	s_nop 1
	v_permlane16_swap_b32_e32 v104, v112
	v_permlane16_swap_b32_e32 v105, v113
	v_permlane16_swap_b32_e32 v106, v114
	v_permlane16_swap_b32_e32 v107, v115
	v_cvt_pk_bf16_f32 v144, v104, v105
	v_cvt_pk_bf16_f32 v145, v106, v107
	v_cvt_pk_bf16_f32 v146, v112, v113
	v_cvt_pk_bf16_f32 v147, v114, v115
	global_store_dwordx4 v[234:235], v[144:147], off offset:256
	v_lshlrev_b32_e32 v140, 16, v180
	v_and_b32_e32 v141, 0xffff0000, v180
	v_lshlrev_b32_e32 v142, 16, v181
	v_and_b32_e32 v143, 0xffff0000, v181
	v_mul_f32_e32 v120, v128, v140
	v_mul_f32_e32 v121, v129, v141
	v_mul_f32_e32 v122, v130, v142
	v_mul_f32_e32 v123, v131, v143
	v_lshlrev_b32_e32 v140, 16, v182
	v_and_b32_e32 v141, 0xffff0000, v182
	v_lshlrev_b32_e32 v142, 16, v183
	v_and_b32_e32 v143, 0xffff0000, v183
	v_mul_f32_e32 v128, v132, v140
	v_mul_f32_e32 v129, v133, v141
	v_mul_f32_e32 v130, v134, v142
	v_mul_f32_e32 v131, v135, v143
	s_nop 1
	v_permlane16_swap_b32_e32 v120, v128
	v_permlane16_swap_b32_e32 v121, v129
	v_permlane16_swap_b32_e32 v122, v130
	v_permlane16_swap_b32_e32 v123, v131
; __device__ __forceinline__ unsigned cvtpk(float lo, float hi) { f32x2_t v = {lo, hi}; bf16x2_t b = __builtin_convertvector(v, bf16x2_t); return __builtin_bit_cast(unsigned, b); }
; __device__ __forceinline__ float bflo(unsigned w) { return __uint_as_float(w << 16); }
; __device__ __forceinline__ float bfhi(unsigned w) { return __uint_as_float(w & 0xffff0000u); }
; __device__ __forceinline__ void phase_merge(const Ptrs& p, LAS unsigned char* lds) {
;     ...
;                 for (int m = 0; m < 4; ++m) { const int row = row0 + ai * 128 + wr * 64 + m * 16 + fr;
; #pragma unroll
;                     for (int bj = 0; bj < 2; ++bj)
; #pragma unroll
;                         for (int n = 0; n < 2; ++n) { const int c = col0 + bj * 128 + wc * 32 + n * 16 + fq * 4; const size_t o = (size_t)row * PLD + c;
;                             const u32x2 sa = *(const u32x2*)(pr + o + C_GA); u32x2 sc = sa; if (seg == 0) sc = *(const u32x2*)(pr + o + C_GC);
;                             f32x4 v = acc[ai][bj][m][n];
;                             const float a0 = bflo(sa.x), a1 = bfhi(sa.x), a2 = bflo(sa.y), a3 = bfhi(sa.y);
;                             if (seg == 0) { v[0] *= bflo(sc.x) * __builtin_amdgcn_rcpf(a0); v[1] *= bfhi(sc.x) * __builtin_amdgcn_rcpf(a1); v[2] *= bflo(sc.y) * __builtin_amdgcn_rcpf(a2); v[3] *= bfhi(sc.y) * __builtin_amdgcn_rcpf(a3); }
;                             else { v[0] *= a0; v[1] *= a1; v[2] *= a2; v[3] *= a3; }
;                             acc[ai][bj][m][n] = v;
;                             if (seg == 1) { u32x2 w; w.x = cvtpk(v[0], v[1]); w.y = cvtpk(v[2], v[3]); *(u32x2*)(mg + (size_t)row * D + c) = w; } }
;                     asm volatile("" ::: "memory"); }
;         }
	v_cvt_pk_bf16_f32 v136, v120, v121
	v_cvt_pk_bf16_f32 v137, v122, v123
	v_cvt_pk_bf16_f32 v138, v128, v129
	v_cvt_pk_bf16_f32 v139, v130, v131
	global_store_dwordx4 v[236:237], v[136:139], off
	v_lshlrev_b32_e32 v140, 16, v184
	v_and_b32_e32 v141, 0xffff0000, v184
	v_lshlrev_b32_e32 v142, 16, v185
	v_and_b32_e32 v143, 0xffff0000, v185
	v_mul_f32_e32 v132, v124, v140
	v_mul_f32_e32 v133, v125, v141
	v_mul_f32_e32 v134, v126, v142
	v_mul_f32_e32 v135, v127, v143
	v_lshlrev_b32_e32 v140, 16, v186
	v_and_b32_e32 v141, 0xffff0000, v186
	v_lshlrev_b32_e32 v142, 16, v187
	v_and_b32_e32 v143, 0xffff0000, v187
	v_mul_f32_e32 v124, v116, v140
	v_mul_f32_e32 v125, v117, v141
	v_mul_f32_e32 v126, v118, v142
	v_mul_f32_e32 v127, v119, v143
	s_nop 1
	v_permlane16_swap_b32_e32 v132, v124
	v_permlane16_swap_b32_e32 v133, v125
	v_permlane16_swap_b32_e32 v134, v126
	v_permlane16_swap_b32_e32 v135, v127
	v_cvt_pk_bf16_f32 v144, v132, v133
	v_cvt_pk_bf16_f32 v145, v134, v135
	v_cvt_pk_bf16_f32 v146, v124, v125
	v_cvt_pk_bf16_f32 v147, v126, v127
	global_store_dwordx4 v[236:237], v[144:147], off offset:256
	v_lshlrev_b32_e32 v140, 16, v188
	v_and_b32_e32 v141, 0xffff0000, v188
	v_lshlrev_b32_e32 v142, 16, v189
	v_and_b32_e32 v143, 0xffff0000, v189
	v_mul_f32_e32 v116, v108, v140
	v_mul_f32_e32 v117, v109, v141
	v_mul_f32_e32 v118, v110, v142
	v_mul_f32_e32 v119, v111, v143
	v_lshlrev_b32_e32 v140, 16, v190
	v_and_b32_e32 v141, 0xffff0000, v190
	v_lshlrev_b32_e32 v142, 16, v191
	v_and_b32_e32 v143, 0xffff0000, v191
	v_mul_f32_e32 v108, v96, v140
	v_mul_f32_e32 v109, v97, v141
	v_mul_f32_e32 v110, v98, v142
	v_mul_f32_e32 v111, v99, v143
	s_nop 1
	v_permlane16_swap_b32_e32 v116, v108
	v_permlane16_swap_b32_e32 v117, v109
	v_permlane16_swap_b32_e32 v118, v110
	v_permlane16_swap_b32_e32 v119, v111
	v_cvt_pk_bf16_f32 v136, v116, v117
	v_cvt_pk_bf16_f32 v137, v118, v119
	v_cvt_pk_bf16_f32 v138, v108, v109
	v_cvt_pk_bf16_f32 v139, v110, v111
	global_store_dwordx4 v[238:239], v[136:139], off
	v_lshlrev_b32_e32 v140, 16, v192
	v_and_b32_e32 v141, 0xffff0000, v192
	v_lshlrev_b32_e32 v142, 16, v193
	v_and_b32_e32 v143, 0xffff0000, v193
	v_mul_f32_e32 v96, v92, v140
	v_mul_f32_e32 v97, v93, v141
	v_mul_f32_e32 v98, v94, v142
	v_mul_f32_e32 v99, v95, v143
	v_lshlrev_b32_e32 v140, 16, v194
	v_and_b32_e32 v141, 0xffff0000, v194
	v_lshlrev_b32_e32 v142, 16, v195
	v_and_b32_e32 v143, 0xffff0000, v195
	v_mul_f32_e32 v92, v84, v140
	v_mul_f32_e32 v93, v85, v141
	v_mul_f32_e32 v94, v86, v142
	v_mul_f32_e32 v95, v87, v143
	s_nop 1
	v_permlane16_swap_b32_e32 v96, v92
	v_permlane16_swap_b32_e32 v97, v93
	v_permlane16_swap_b32_e32 v98, v94
	v_permlane16_swap_b32_e32 v99, v95
	v_cvt_pk_bf16_f32 v144, v96, v97
	v_cvt_pk_bf16_f32 v145, v98, v99
	v_cvt_pk_bf16_f32 v146, v92, v93
	v_cvt_pk_bf16_f32 v147, v94, v95
	global_store_dwordx4 v[238:239], v[144:147], off offset:256
	v_lshlrev_b32_e32 v140, 16, v196
	v_and_b32_e32 v141, 0xffff0000, v196
	v_lshlrev_b32_e32 v142, 16, v197
	v_and_b32_e32 v143, 0xffff0000, v197
	v_mul_f32_e32 v84, v76, v140
	v_mul_f32_e32 v85, v77, v141
	v_mul_f32_e32 v86, v78, v142
	v_mul_f32_e32 v87, v79, v143
	v_lshlrev_b32_e32 v140, 16, v198
	v_and_b32_e32 v141, 0xffff0000, v198
	v_lshlrev_b32_e32 v142, 16, v199
	v_and_b32_e32 v143, 0xffff0000, v199
	v_mul_f32_e32 v76, v64, v140
	v_mul_f32_e32 v77, v65, v141
	v_mul_f32_e32 v78, v66, v142
	v_mul_f32_e32 v79, v67, v143
	s_nop 1
	v_permlane16_swap_b32_e32 v84, v76
	v_permlane16_swap_b32_e32 v85, v77
	v_permlane16_swap_b32_e32 v86, v78
	v_permlane16_swap_b32_e32 v87, v79
	v_cvt_pk_bf16_f32 v136, v84, v85
	v_cvt_pk_bf16_f32 v137, v86, v87
	v_cvt_pk_bf16_f32 v138, v76, v77
	v_cvt_pk_bf16_f32 v139, v78, v79
	global_store_dwordx4 v[240:241], v[136:139], off
	v_lshlrev_b32_e32 v140, 16, v200
	v_and_b32_e32 v141, 0xffff0000, v200
	v_lshlrev_b32_e32 v142, 16, v201
	v_and_b32_e32 v143, 0xffff0000, v201
	v_mul_f32_e32 v64, v60, v140
	v_mul_f32_e32 v65, v61, v141
	v_mul_f32_e32 v66, v62, v142
	v_mul_f32_e32 v67, v63, v143
	v_lshlrev_b32_e32 v140, 16, v202
	v_and_b32_e32 v141, 0xffff0000, v202
	v_lshlrev_b32_e32 v142, 16, v203
	v_and_b32_e32 v143, 0xffff0000, v203
	v_mul_f32_e32 v60, v52, v140
	v_mul_f32_e32 v61, v53, v141
	v_mul_f32_e32 v62, v54, v142
	v_mul_f32_e32 v63, v55, v143
	s_nop 1
	v_permlane16_swap_b32_e32 v64, v60
	v_permlane16_swap_b32_e32 v65, v61
	v_permlane16_swap_b32_e32 v66, v62
	v_permlane16_swap_b32_e32 v67, v63
	v_cvt_pk_bf16_f32 v144, v64, v65
	v_cvt_pk_bf16_f32 v145, v66, v67
	v_cvt_pk_bf16_f32 v146, v60, v61
	v_cvt_pk_bf16_f32 v147, v62, v63
	global_store_dwordx4 v[240:241], v[144:147], off offset:256
	v_lshlrev_b32_e32 v140, 16, v204
	v_and_b32_e32 v141, 0xffff0000, v204
	v_lshlrev_b32_e32 v142, 16, v205
	v_and_b32_e32 v143, 0xffff0000, v205
	v_mul_f32_e32 v52, v44, v140
	v_mul_f32_e32 v53, v45, v141
	v_mul_f32_e32 v54, v46, v142
	v_mul_f32_e32 v55, v47, v143
	v_lshlrev_b32_e32 v140, 16, v206
	v_and_b32_e32 v141, 0xffff0000, v206
	v_lshlrev_b32_e32 v142, 16, v207
	v_and_b32_e32 v143, 0xffff0000, v207
	v_mul_f32_e32 v44, v32, v140
	v_mul_f32_e32 v45, v33, v141
	v_mul_f32_e32 v46, v34, v142
	v_mul_f32_e32 v47, v35, v143
	s_nop 1
	v_permlane16_swap_b32_e32 v52, v44
	v_permlane16_swap_b32_e32 v53, v45
	v_permlane16_swap_b32_e32 v54, v46
	v_permlane16_swap_b32_e32 v55, v47
	v_cvt_pk_bf16_f32 v136, v52, v53
	v_cvt_pk_bf16_f32 v137, v54, v55
	v_cvt_pk_bf16_f32 v138, v44, v45
	v_cvt_pk_bf16_f32 v139, v46, v47
	global_store_dwordx4 v[242:243], v[136:139], off
	v_lshlrev_b32_e32 v140, 16, v208
	v_and_b32_e32 v141, 0xffff0000, v208
	v_lshlrev_b32_e32 v142, 16, v209
	v_and_b32_e32 v143, 0xffff0000, v209
	v_mul_f32_e32 v32, v28, v140
	v_mul_f32_e32 v33, v29, v141
	v_mul_f32_e32 v34, v30, v142
	v_mul_f32_e32 v35, v31, v143
	v_lshlrev_b32_e32 v140, 16, v210
	v_and_b32_e32 v141, 0xffff0000, v210
	v_lshlrev_b32_e32 v142, 16, v211
	v_and_b32_e32 v143, 0xffff0000, v211
	v_mul_f32_e32 v28, v20, v140
	v_mul_f32_e32 v29, v21, v141
	v_mul_f32_e32 v30, v22, v142
	v_mul_f32_e32 v31, v23, v143
	s_nop 1
	v_permlane16_swap_b32_e32 v32, v28
	v_permlane16_swap_b32_e32 v33, v29
	v_permlane16_swap_b32_e32 v34, v30
	v_permlane16_swap_b32_e32 v35, v31
	v_cvt_pk_bf16_f32 v144, v32, v33
	v_cvt_pk_bf16_f32 v145, v34, v35
	v_cvt_pk_bf16_f32 v146, v28, v29
	v_cvt_pk_bf16_f32 v147, v30, v31
	global_store_dwordx4 v[242:243], v[144:147], off offset:256
	s_branch .LBB0_510
